# WcsT fold accumulation loop software-pipelined: w_fmix loads of block b+1 issued before the FMAs of block b (two register sets)
# speedup vs baseline: 1.0080x; 1.0080x over previous
; __device__ void phase_prep(KParams& p, int bid, int nb, char* smem) {
;     ...
;     for (int i = vb * NTHREADS + tid; i < 4 * 64 * 256; i += nb * NTHREADS) {
;       const int d = i & 255, cg = (i >> 8) & 63, g = i >> 14;
;       float c0_ = 0.f, c1_ = 0.f, c2_ = 0.f, c3_ = 0.f, s0_ = 0.f, s1_ = 0.f, s2_ = 0.f, s3_ = 0.f;
;       const float* wp = p.w_fmix + (size_t)g * 65536 + d;
; #pragma unroll 1
;       for (int mb = 0; mb < 256; mb += 16) {
;         float wv[16];
; #pragma unroll
;         for (int mm = 0; mm < 16; ++mm) wv[mm] = wp[(mb + mm) * 256];
; #pragma unroll
;         for (int mm = 0; mm < 16; ++mm) {
;           const int m = mb + mm;
;           const int p0 = (m * (cg * 4 + 0)) & 255, p1 = (m * (cg * 4 + 1)) & 255, p2 = (m * (cg * 4 + 2)) & 255, p3 = (m * (cg * 4 + 3)) & 255;
;           c0_ += t256[p0] * wv[mm]; s0_ += t256[(p0 - 64) & 255] * wv[mm];
;           c1_ += t256[p1] * wv[mm]; s1_ += t256[(p1 - 64) & 255] * wv[mm];
;           c2_ += t256[p2] * wv[mm]; s2_ += t256[(p2 - 64) & 255] * wv[mm];
;           c3_ += t256[p3] * wv[mm]; s3_ += t256[(p3 - 64) & 255] * wv[mm];
;         }
;       }
.LBB0_50:
	v_ashrrev_i32_e32 v10, 14, v1
	v_bfe_u32 v2, v1, 8, 6
	v_ashrrev_i32_e32 v11, 31, v10
	v_lshlrev_b32_e32 v31, 6, v2
	v_lshlrev_b64 v[10:11], 18, v[10:11]
	v_or_b32_e32 v33, 16, v31
	v_or_b32_e32 v35, 32, v31
	v_or_b32_e32 v37, 48, v31
	v_mul_u32_u24_e32 v39, 60, v2
	v_mul_u32_u24_e32 v41, 56, v2
	v_mul_u32_u24_e32 v43, 52, v2
	v_mul_u32_u24_e32 v45, 48, v2
	v_mul_u32_u24_e32 v47, 44, v2
	v_mul_u32_u24_e32 v49, 40, v2
	v_mul_u32_u24_e32 v51, 36, v2
	v_lshlrev_b32_e32 v52, 5, v2
	v_mul_u32_u24_e32 v53, 28, v2
	v_mul_u32_u24_e32 v54, 24, v2
	v_mul_u32_u24_e32 v55, 20, v2
	v_lshlrev_b32_e32 v56, 4, v2
	v_mul_u32_u24_e32 v57, 12, v2
	v_lshlrev_b32_e32 v58, 3, v2
	v_lshlrev_b32_e32 v59, 2, v2
	v_lshl_add_u64 v[12:13], v[8:9], 0, v[10:11]
	v_mov_b32_e32 v60, 0
	v_mov_b32_e32 v61, 0
	v_mov_b32_e32 v62, 0
	v_mov_b32_e32 v63, 0
	s_mov_b32 s19, 0
	v_mov_b32_e32 v14, 0
	v_mov_b32_e32 v15, v3
	v_mov_b32_e32 v16, 0
	v_mov_b32_e32 v17, v3
	v_mov_b32_e32 v18, 0
	v_mov_b32_e32 v19, v3
	v_mov_b32_e32 v20, 0
	v_mov_b32_e32 v21, v3
	v_lshlrev_b32_e32 v60, 2, v2
	v_mul_u32_u24_e32 v61, v60, v0
	v_add_u32_e32 v62, v61, v0
	v_add_u32_e32 v63, v62, v0
	v_add_u32_e32 v64, v63, v0
	v_and_b32_e32 v65, 0xff, v61
	v_add_u32_e32 v66, 0xc0, v61
	v_lshlrev_b32_e32 v65, 2, v65
	v_and_b32_e32 v66, 0xff, v66
	v_lshlrev_b32_e32 v66, 2, v66
	v_and_b32_e32 v67, 0xff, v62
	v_add_u32_e32 v68, 0xc0, v62
	v_lshlrev_b32_e32 v67, 2, v67
	v_and_b32_e32 v68, 0xff, v68
	v_lshlrev_b32_e32 v68, 2, v68
	v_and_b32_e32 v69, 0xff, v63
	v_add_u32_e32 v70, 0xc0, v63
	v_lshlrev_b32_e32 v69, 2, v69
	v_and_b32_e32 v70, 0xff, v70
	v_lshlrev_b32_e32 v70, 2, v70
	v_and_b32_e32 v71, 0xff, v64
	v_add_u32_e32 v72, 0xc0, v64
	v_lshlrev_b32_e32 v71, 2, v71
	v_and_b32_e32 v72, 0xff, v72
	v_lshlrev_b32_e32 v72, 2, v72
	ds_read_b32 v74, v65 offset:20480
	ds_read_b32 v75, v67 offset:20480
	ds_read_b32 v76, v66 offset:20480
	ds_read_b32 v77, v68 offset:20480
	ds_read_b32 v78, v69 offset:20480
	ds_read_b32 v79, v71 offset:20480
	ds_read_b32 v80, v70 offset:20480
	ds_read_b32 v81, v72 offset:20480
	v_lshlrev_b32_e32 v60, 5, v0
	s_waitcnt lgkmcnt(0)
	s_barrier
	ds_write_b128 v60, v[74:77] offset:32768
	ds_write_b128 v60, v[78:81] offset:32784
	s_waitcnt lgkmcnt(0)
	s_barrier
	v_mov_b32_e32 v60, 0
	v_add_co_u32_e32 v26, vcc, s15, v12
	s_nop 1
	v_addc_co_u32_e32 v27, vcc, -1, v13, vcc
	v_add_co_u32_e32 v24, vcc, s16, v12
	s_nop 1
	v_addc_co_u32_e32 v25, vcc, -1, v13, vcc
	v_add_co_u32_e32 v28, vcc, s17, v12
	s_nop 1
	v_addc_co_u32_e32 v29, vcc, -1, v13, vcc
	global_load_dword v22, v[12:13], off offset:-1024
	global_load_dword v2, v[12:13], off
	global_load_dword v50, v[26:27], off offset:-3072
	global_load_dword v48, v[26:27], off offset:-2048
	global_load_dword v44, v[26:27], off offset:-1024
	global_load_dword v34, v[28:29], off offset:-3072
	global_load_dword v32, v[28:29], off offset:-2048
	s_nop 0
	global_load_dword v28, v[28:29], off offset:-1024
	s_nop 0
	global_load_dword v46, v[24:25], off offset:-4096
	global_load_dword v42, v[24:25], off offset:-3072
	global_load_dword v40, v[24:25], off offset:-2048
	global_load_dword v38, v[24:25], off offset:-1024
	global_load_dword v36, v[24:25], off
	global_load_dword v30, v[12:13], off offset:-4096
	global_load_dword v26, v[12:13], off offset:-3072
	s_nop 0
	global_load_dword v24, v[12:13], off offset:-2048
	v_lshl_add_u64 v[12:13], v[12:13], 0, s[10:11]
	s_mov_b32 s19, 0
.LBB0_51:
	v_add_co_u32_e32 v228, vcc, s15, v12
	s_nop 1
	v_addc_co_u32_e32 v229, vcc, -1, v13, vcc
	v_add_co_u32_e32 v230, vcc, s16, v12
	s_nop 1
	v_addc_co_u32_e32 v231, vcc, -1, v13, vcc
	v_add_co_u32_e32 v232, vcc, s17, v12
	s_nop 1
	v_addc_co_u32_e32 v233, vcc, -1, v13, vcc
	global_load_dword v226, v[12:13], off offset:-1024
	global_load_dword v227, v[12:13], off
	global_load_dword v212, v[228:229], off offset:-3072
	global_load_dword v213, v[228:229], off offset:-2048
	global_load_dword v214, v[228:229], off offset:-1024
	global_load_dword v220, v[232:233], off offset:-3072
	global_load_dword v221, v[232:233], off offset:-2048
	s_nop 0
	global_load_dword v222, v[232:233], off offset:-1024
	s_nop 0
	global_load_dword v215, v[230:231], off offset:-4096
	global_load_dword v216, v[230:231], off offset:-3072
	global_load_dword v217, v[230:231], off offset:-2048
	global_load_dword v218, v[230:231], off offset:-1024
	global_load_dword v219, v[230:231], off
	global_load_dword v223, v[12:13], off offset:-4096
	global_load_dword v224, v[12:13], off offset:-3072
	s_nop 0
	global_load_dword v225, v[12:13], off offset:-2048
	v_lshl_add_u64 v[12:13], v[12:13], 0, s[10:11]
	ds_read_b128 v[64:67], v60 offset:32768
	ds_read_b128 v[68:71], v60 offset:32784
	ds_read_b128 v[72:75], v60 offset:32800
	ds_read_b128 v[76:79], v60 offset:32816
	ds_read_b128 v[80:83], v60 offset:32832
	ds_read_b128 v[84:87], v60 offset:32848
	ds_read_b128 v[88:91], v60 offset:32864
	ds_read_b128 v[92:95], v60 offset:32880
	ds_read_b128 v[96:99], v60 offset:32896
	ds_read_b128 v[100:103], v60 offset:32912
	ds_read_b128 v[104:107], v60 offset:32928
	ds_read_b128 v[108:111], v60 offset:32944
	ds_read_b128 v[112:115], v60 offset:32960
	ds_read_b128 v[116:119], v60 offset:32976
	ds_read_b128 v[120:123], v60 offset:32992
	ds_read_b128 v[124:127], v60 offset:33008
	ds_read_b128 v[128:131], v60 offset:33024
	ds_read_b128 v[132:135], v60 offset:33040
	ds_read_b128 v[136:139], v60 offset:33056
	ds_read_b128 v[140:143], v60 offset:33072
	ds_read_b128 v[144:147], v60 offset:33088
	ds_read_b128 v[148:151], v60 offset:33104
	ds_read_b128 v[152:155], v60 offset:33120
	ds_read_b128 v[156:159], v60 offset:33136
	ds_read_b128 v[160:163], v60 offset:33152
	ds_read_b128 v[164:167], v60 offset:33168
	ds_read_b128 v[168:171], v60 offset:33184
	ds_read_b128 v[172:175], v60 offset:33200
	ds_read_b128 v[196:199], v60 offset:33216
	ds_read_b128 v[200:203], v60 offset:33232
	ds_read_b128 v[204:207], v60 offset:33248
	ds_read_b128 v[208:211], v60 offset:33264
	v_add_u32_e32 v60, 0x200, v60
	s_waitcnt vmcnt(16) lgkmcnt(0)
; __device__ void phase_prep(KParams& p, int bid, int nb, char* smem) {
;     ...
;       for (int mb = 0; mb < 256; mb += 16) {
;         float wv[16];
; #pragma unroll
;         for (int mm = 0; mm < 16; ++mm) wv[mm] = wp[(mb + mm) * 256];
; #pragma unroll
;         for (int mm = 0; mm < 16; ++mm) {
;           const int m = mb + mm;
;           const int p0 = (m * (cg * 4 + 0)) & 255, p1 = (m * (cg * 4 + 1)) & 255, p2 = (m * (cg * 4 + 2)) & 255, p3 = (m * (cg * 4 + 3)) & 255;
;           c0_ += t256[p0] * wv[mm]; s0_ += t256[(p0 - 64) & 255] * wv[mm];
;           c1_ += t256[p1] * wv[mm]; s1_ += t256[(p1 - 64) & 255] * wv[mm];
;           c2_ += t256[p2] * wv[mm]; s2_ += t256[(p2 - 64) & 255] * wv[mm];
;           c3_ += t256[p3] * wv[mm]; s3_ += t256[(p3 - 64) & 255] * wv[mm];
;         }
	v_pk_fma_f32 v[20:21], v[50:51], v[64:65], v[20:21] op_sel_hi:[0,1,1]
	v_pk_fma_f32 v[18:19], v[50:51], v[66:67], v[18:19] op_sel_hi:[0,1,1]
	v_pk_fma_f32 v[16:17], v[50:51], v[68:69], v[16:17] op_sel_hi:[0,1,1]
	v_pk_fma_f32 v[14:15], v[50:51], v[70:71], v[14:15] op_sel_hi:[0,1,1]
	v_pk_fma_f32 v[20:21], v[48:49], v[72:73], v[20:21] op_sel_hi:[0,1,1]
	v_pk_fma_f32 v[18:19], v[48:49], v[74:75], v[18:19] op_sel_hi:[0,1,1]
	v_pk_fma_f32 v[16:17], v[48:49], v[76:77], v[16:17] op_sel_hi:[0,1,1]
	v_pk_fma_f32 v[14:15], v[48:49], v[78:79], v[14:15] op_sel_hi:[0,1,1]
	v_pk_fma_f32 v[20:21], v[44:45], v[80:81], v[20:21] op_sel_hi:[0,1,1]
	v_pk_fma_f32 v[18:19], v[44:45], v[82:83], v[18:19] op_sel_hi:[0,1,1]
	v_pk_fma_f32 v[16:17], v[44:45], v[84:85], v[16:17] op_sel_hi:[0,1,1]
	v_pk_fma_f32 v[14:15], v[44:45], v[86:87], v[14:15] op_sel_hi:[0,1,1]
	v_pk_fma_f32 v[20:21], v[46:47], v[88:89], v[20:21] op_sel_hi:[0,1,1]
	v_pk_fma_f32 v[18:19], v[46:47], v[90:91], v[18:19] op_sel_hi:[0,1,1]
	v_pk_fma_f32 v[16:17], v[46:47], v[92:93], v[16:17] op_sel_hi:[0,1,1]
	v_pk_fma_f32 v[14:15], v[46:47], v[94:95], v[14:15] op_sel_hi:[0,1,1]
	v_pk_fma_f32 v[20:21], v[42:43], v[96:97], v[20:21] op_sel_hi:[0,1,1]
	v_pk_fma_f32 v[18:19], v[42:43], v[98:99], v[18:19] op_sel_hi:[0,1,1]
	v_pk_fma_f32 v[16:17], v[42:43], v[100:101], v[16:17] op_sel_hi:[0,1,1]
	v_pk_fma_f32 v[14:15], v[42:43], v[102:103], v[14:15] op_sel_hi:[0,1,1]
	v_pk_fma_f32 v[20:21], v[40:41], v[104:105], v[20:21] op_sel_hi:[0,1,1]
	v_pk_fma_f32 v[18:19], v[40:41], v[106:107], v[18:19] op_sel_hi:[0,1,1]
	v_pk_fma_f32 v[16:17], v[40:41], v[108:109], v[16:17] op_sel_hi:[0,1,1]
	v_pk_fma_f32 v[14:15], v[40:41], v[110:111], v[14:15] op_sel_hi:[0,1,1]
	v_pk_fma_f32 v[20:21], v[38:39], v[112:113], v[20:21] op_sel_hi:[0,1,1]
	v_pk_fma_f32 v[18:19], v[38:39], v[114:115], v[18:19] op_sel_hi:[0,1,1]
	v_pk_fma_f32 v[16:17], v[38:39], v[116:117], v[16:17] op_sel_hi:[0,1,1]
	v_pk_fma_f32 v[14:15], v[38:39], v[118:119], v[14:15] op_sel_hi:[0,1,1]
	v_pk_fma_f32 v[20:21], v[36:37], v[120:121], v[20:21] op_sel_hi:[0,1,1]
	v_pk_fma_f32 v[18:19], v[36:37], v[122:123], v[18:19] op_sel_hi:[0,1,1]
	v_pk_fma_f32 v[16:17], v[36:37], v[124:125], v[16:17] op_sel_hi:[0,1,1]
	v_pk_fma_f32 v[14:15], v[36:37], v[126:127], v[14:15] op_sel_hi:[0,1,1]
	v_pk_fma_f32 v[20:21], v[34:35], v[128:129], v[20:21] op_sel_hi:[0,1,1]
	v_pk_fma_f32 v[18:19], v[34:35], v[130:131], v[18:19] op_sel_hi:[0,1,1]
	v_pk_fma_f32 v[16:17], v[34:35], v[132:133], v[16:17] op_sel_hi:[0,1,1]
	v_pk_fma_f32 v[14:15], v[34:35], v[134:135], v[14:15] op_sel_hi:[0,1,1]
	v_pk_fma_f32 v[20:21], v[32:33], v[136:137], v[20:21] op_sel_hi:[0,1,1]
	v_pk_fma_f32 v[18:19], v[32:33], v[138:139], v[18:19] op_sel_hi:[0,1,1]
	v_pk_fma_f32 v[16:17], v[32:33], v[140:141], v[16:17] op_sel_hi:[0,1,1]
	v_pk_fma_f32 v[14:15], v[32:33], v[142:143], v[14:15] op_sel_hi:[0,1,1]
	v_pk_fma_f32 v[20:21], v[28:29], v[144:145], v[20:21] op_sel_hi:[0,1,1]
	v_pk_fma_f32 v[18:19], v[28:29], v[146:147], v[18:19] op_sel_hi:[0,1,1]
	v_pk_fma_f32 v[16:17], v[28:29], v[148:149], v[16:17] op_sel_hi:[0,1,1]
	v_pk_fma_f32 v[14:15], v[28:29], v[150:151], v[14:15] op_sel_hi:[0,1,1]
	v_pk_fma_f32 v[20:21], v[30:31], v[152:153], v[20:21] op_sel_hi:[0,1,1]
	v_pk_fma_f32 v[18:19], v[30:31], v[154:155], v[18:19] op_sel_hi:[0,1,1]
	v_pk_fma_f32 v[16:17], v[30:31], v[156:157], v[16:17] op_sel_hi:[0,1,1]
	v_pk_fma_f32 v[14:15], v[30:31], v[158:159], v[14:15] op_sel_hi:[0,1,1]
	v_pk_fma_f32 v[20:21], v[26:27], v[160:161], v[20:21] op_sel_hi:[0,1,1]
	v_pk_fma_f32 v[18:19], v[26:27], v[162:163], v[18:19] op_sel_hi:[0,1,1]
	v_pk_fma_f32 v[16:17], v[26:27], v[164:165], v[16:17] op_sel_hi:[0,1,1]
	v_pk_fma_f32 v[14:15], v[26:27], v[166:167], v[14:15] op_sel_hi:[0,1,1]
	v_pk_fma_f32 v[20:21], v[24:25], v[168:169], v[20:21] op_sel_hi:[0,1,1]
	v_pk_fma_f32 v[18:19], v[24:25], v[170:171], v[18:19] op_sel_hi:[0,1,1]
	v_pk_fma_f32 v[16:17], v[24:25], v[172:173], v[16:17] op_sel_hi:[0,1,1]
	v_pk_fma_f32 v[14:15], v[24:25], v[174:175], v[14:15] op_sel_hi:[0,1,1]
	v_pk_fma_f32 v[20:21], v[22:23], v[196:197], v[20:21] op_sel_hi:[0,1,1]
	v_pk_fma_f32 v[18:19], v[22:23], v[198:199], v[18:19] op_sel_hi:[0,1,1]
	v_pk_fma_f32 v[16:17], v[22:23], v[200:201], v[16:17] op_sel_hi:[0,1,1]
	v_pk_fma_f32 v[14:15], v[22:23], v[202:203], v[14:15] op_sel_hi:[0,1,1]
	v_pk_fma_f32 v[20:21], v[2:3], v[204:205], v[20:21] op_sel_hi:[0,1,1]
	v_pk_fma_f32 v[18:19], v[2:3], v[206:207], v[18:19] op_sel_hi:[0,1,1]
	v_pk_fma_f32 v[16:17], v[2:3], v[208:209], v[16:17] op_sel_hi:[0,1,1]
	v_pk_fma_f32 v[14:15], v[2:3], v[210:211], v[14:15] op_sel_hi:[0,1,1]
	v_add_co_u32_e32 v26, vcc, s15, v12
	s_nop 1
	v_addc_co_u32_e32 v27, vcc, -1, v13, vcc
	v_add_co_u32_e32 v24, vcc, s16, v12
	s_nop 1
	v_addc_co_u32_e32 v25, vcc, -1, v13, vcc
	v_add_co_u32_e32 v28, vcc, s17, v12
	s_nop 1
	v_addc_co_u32_e32 v29, vcc, -1, v13, vcc
	global_load_dword v22, v[12:13], off offset:-1024
	global_load_dword v2, v[12:13], off
	global_load_dword v50, v[26:27], off offset:-3072
	global_load_dword v48, v[26:27], off offset:-2048
	global_load_dword v44, v[26:27], off offset:-1024
	global_load_dword v34, v[28:29], off offset:-3072
	global_load_dword v32, v[28:29], off offset:-2048
	s_nop 0
	global_load_dword v28, v[28:29], off offset:-1024
	s_nop 0
	global_load_dword v46, v[24:25], off offset:-4096
	global_load_dword v42, v[24:25], off offset:-3072
	global_load_dword v40, v[24:25], off offset:-2048
	global_load_dword v38, v[24:25], off offset:-1024
	global_load_dword v36, v[24:25], off
	global_load_dword v30, v[12:13], off offset:-4096
	global_load_dword v26, v[12:13], off offset:-3072
; __device__ void phase_prep(KParams& p, int bid, int nb, char* smem) {
;     ...
;       for (int mb = 0; mb < 256; mb += 16) {
;         float wv[16];
; #pragma unroll
;         for (int mm = 0; mm < 16; ++mm) wv[mm] = wp[(mb + mm) * 256];
; #pragma unroll
;         for (int mm = 0; mm < 16; ++mm) {
;           const int m = mb + mm;
;           const int p0 = (m * (cg * 4 + 0)) & 255, p1 = (m * (cg * 4 + 1)) & 255, p2 = (m * (cg * 4 + 2)) & 255, p3 = (m * (cg * 4 + 3)) & 255;
;           c0_ += t256[p0] * wv[mm]; s0_ += t256[(p0 - 64) & 255] * wv[mm];
;           c1_ += t256[p1] * wv[mm]; s1_ += t256[(p1 - 64) & 255] * wv[mm];
;           c2_ += t256[p2] * wv[mm]; s2_ += t256[(p2 - 64) & 255] * wv[mm];
;           c3_ += t256[p3] * wv[mm]; s3_ += t256[(p3 - 64) & 255] * wv[mm];
;         }
	s_nop 0
	global_load_dword v24, v[12:13], off offset:-2048
	v_lshl_add_u64 v[12:13], v[12:13], 0, s[10:11]
	ds_read_b128 v[64:67], v60 offset:32768
	ds_read_b128 v[68:71], v60 offset:32784
	ds_read_b128 v[72:75], v60 offset:32800
	ds_read_b128 v[76:79], v60 offset:32816
	ds_read_b128 v[80:83], v60 offset:32832
	ds_read_b128 v[84:87], v60 offset:32848
	ds_read_b128 v[88:91], v60 offset:32864
	ds_read_b128 v[92:95], v60 offset:32880
	ds_read_b128 v[96:99], v60 offset:32896
	ds_read_b128 v[100:103], v60 offset:32912
	ds_read_b128 v[104:107], v60 offset:32928
	ds_read_b128 v[108:111], v60 offset:32944
	ds_read_b128 v[112:115], v60 offset:32960
	ds_read_b128 v[116:119], v60 offset:32976
	ds_read_b128 v[120:123], v60 offset:32992
	ds_read_b128 v[124:127], v60 offset:33008
	ds_read_b128 v[128:131], v60 offset:33024
	ds_read_b128 v[132:135], v60 offset:33040
	ds_read_b128 v[136:139], v60 offset:33056
	ds_read_b128 v[140:143], v60 offset:33072
	ds_read_b128 v[144:147], v60 offset:33088
	ds_read_b128 v[148:151], v60 offset:33104
	ds_read_b128 v[152:155], v60 offset:33120
	ds_read_b128 v[156:159], v60 offset:33136
	ds_read_b128 v[160:163], v60 offset:33152
	ds_read_b128 v[164:167], v60 offset:33168
	ds_read_b128 v[168:171], v60 offset:33184
	ds_read_b128 v[172:175], v60 offset:33200
	ds_read_b128 v[196:199], v60 offset:33216
	ds_read_b128 v[200:203], v60 offset:33232
	ds_read_b128 v[204:207], v60 offset:33248
	ds_read_b128 v[208:211], v60 offset:33264
	v_add_u32_e32 v60, 0x200, v60
	s_waitcnt vmcnt(16) lgkmcnt(0)
	v_pk_fma_f32 v[20:21], v[212:213], v[64:65], v[20:21] op_sel_hi:[0,1,1]
	v_pk_fma_f32 v[18:19], v[212:213], v[66:67], v[18:19] op_sel_hi:[0,1,1]
	v_pk_fma_f32 v[16:17], v[212:213], v[68:69], v[16:17] op_sel_hi:[0,1,1]
	v_pk_fma_f32 v[14:15], v[212:213], v[70:71], v[14:15] op_sel_hi:[0,1,1]
	v_pk_fma_f32 v[20:21], v[212:213], v[72:73], v[20:21] op_sel:[1,0,0] op_sel_hi:[1,1,1]
	v_pk_fma_f32 v[18:19], v[212:213], v[74:75], v[18:19] op_sel:[1,0,0] op_sel_hi:[1,1,1]
	v_pk_fma_f32 v[16:17], v[212:213], v[76:77], v[16:17] op_sel:[1,0,0] op_sel_hi:[1,1,1]
	v_pk_fma_f32 v[14:15], v[212:213], v[78:79], v[14:15] op_sel:[1,0,0] op_sel_hi:[1,1,1]
	v_pk_fma_f32 v[20:21], v[214:215], v[80:81], v[20:21] op_sel_hi:[0,1,1]
	v_pk_fma_f32 v[18:19], v[214:215], v[82:83], v[18:19] op_sel_hi:[0,1,1]
	v_pk_fma_f32 v[16:17], v[214:215], v[84:85], v[16:17] op_sel_hi:[0,1,1]
	v_pk_fma_f32 v[14:15], v[214:215], v[86:87], v[14:15] op_sel_hi:[0,1,1]
	v_pk_fma_f32 v[20:21], v[214:215], v[88:89], v[20:21] op_sel:[1,0,0] op_sel_hi:[1,1,1]
	v_pk_fma_f32 v[18:19], v[214:215], v[90:91], v[18:19] op_sel:[1,0,0] op_sel_hi:[1,1,1]
	v_pk_fma_f32 v[16:17], v[214:215], v[92:93], v[16:17] op_sel:[1,0,0] op_sel_hi:[1,1,1]
	v_pk_fma_f32 v[14:15], v[214:215], v[94:95], v[14:15] op_sel:[1,0,0] op_sel_hi:[1,1,1]
	v_pk_fma_f32 v[20:21], v[216:217], v[96:97], v[20:21] op_sel_hi:[0,1,1]
	v_pk_fma_f32 v[18:19], v[216:217], v[98:99], v[18:19] op_sel_hi:[0,1,1]
	v_pk_fma_f32 v[16:17], v[216:217], v[100:101], v[16:17] op_sel_hi:[0,1,1]
	v_pk_fma_f32 v[14:15], v[216:217], v[102:103], v[14:15] op_sel_hi:[0,1,1]
	v_pk_fma_f32 v[20:21], v[216:217], v[104:105], v[20:21] op_sel:[1,0,0] op_sel_hi:[1,1,1]
	v_pk_fma_f32 v[18:19], v[216:217], v[106:107], v[18:19] op_sel:[1,0,0] op_sel_hi:[1,1,1]
	v_pk_fma_f32 v[16:17], v[216:217], v[108:109], v[16:17] op_sel:[1,0,0] op_sel_hi:[1,1,1]
	v_pk_fma_f32 v[14:15], v[216:217], v[110:111], v[14:15] op_sel:[1,0,0] op_sel_hi:[1,1,1]
	v_pk_fma_f32 v[20:21], v[218:219], v[112:113], v[20:21] op_sel_hi:[0,1,1]
	v_pk_fma_f32 v[18:19], v[218:219], v[114:115], v[18:19] op_sel_hi:[0,1,1]
	v_pk_fma_f32 v[16:17], v[218:219], v[116:117], v[16:17] op_sel_hi:[0,1,1]
	v_pk_fma_f32 v[14:15], v[218:219], v[118:119], v[14:15] op_sel_hi:[0,1,1]
	v_pk_fma_f32 v[20:21], v[218:219], v[120:121], v[20:21] op_sel:[1,0,0] op_sel_hi:[1,1,1]
	v_pk_fma_f32 v[18:19], v[218:219], v[122:123], v[18:19] op_sel:[1,0,0] op_sel_hi:[1,1,1]
	v_pk_fma_f32 v[16:17], v[218:219], v[124:125], v[16:17] op_sel:[1,0,0] op_sel_hi:[1,1,1]
	v_pk_fma_f32 v[14:15], v[218:219], v[126:127], v[14:15] op_sel:[1,0,0] op_sel_hi:[1,1,1]
	v_pk_fma_f32 v[20:21], v[220:221], v[128:129], v[20:21] op_sel_hi:[0,1,1]
	v_pk_fma_f32 v[18:19], v[220:221], v[130:131], v[18:19] op_sel_hi:[0,1,1]
	v_pk_fma_f32 v[16:17], v[220:221], v[132:133], v[16:17] op_sel_hi:[0,1,1]
	v_pk_fma_f32 v[14:15], v[220:221], v[134:135], v[14:15] op_sel_hi:[0,1,1]
	v_pk_fma_f32 v[20:21], v[220:221], v[136:137], v[20:21] op_sel:[1,0,0] op_sel_hi:[1,1,1]
	v_pk_fma_f32 v[18:19], v[220:221], v[138:139], v[18:19] op_sel:[1,0,0] op_sel_hi:[1,1,1]
	v_pk_fma_f32 v[16:17], v[220:221], v[140:141], v[16:17] op_sel:[1,0,0] op_sel_hi:[1,1,1]
	v_pk_fma_f32 v[14:15], v[220:221], v[142:143], v[14:15] op_sel:[1,0,0] op_sel_hi:[1,1,1]
	v_pk_fma_f32 v[20:21], v[222:223], v[144:145], v[20:21] op_sel_hi:[0,1,1]
	v_pk_fma_f32 v[18:19], v[222:223], v[146:147], v[18:19] op_sel_hi:[0,1,1]
	v_pk_fma_f32 v[16:17], v[222:223], v[148:149], v[16:17] op_sel_hi:[0,1,1]
	v_pk_fma_f32 v[14:15], v[222:223], v[150:151], v[14:15] op_sel_hi:[0,1,1]
	v_pk_fma_f32 v[20:21], v[222:223], v[152:153], v[20:21] op_sel:[1,0,0] op_sel_hi:[1,1,1]
	v_pk_fma_f32 v[18:19], v[222:223], v[154:155], v[18:19] op_sel:[1,0,0] op_sel_hi:[1,1,1]
	v_pk_fma_f32 v[16:17], v[222:223], v[156:157], v[16:17] op_sel:[1,0,0] op_sel_hi:[1,1,1]
	v_pk_fma_f32 v[14:15], v[222:223], v[158:159], v[14:15] op_sel:[1,0,0] op_sel_hi:[1,1,1]
	v_pk_fma_f32 v[20:21], v[224:225], v[160:161], v[20:21] op_sel_hi:[0,1,1]
	v_pk_fma_f32 v[18:19], v[224:225], v[162:163], v[18:19] op_sel_hi:[0,1,1]
	v_pk_fma_f32 v[16:17], v[224:225], v[164:165], v[16:17] op_sel_hi:[0,1,1]
	v_pk_fma_f32 v[14:15], v[224:225], v[166:167], v[14:15] op_sel_hi:[0,1,1]
	v_pk_fma_f32 v[20:21], v[224:225], v[168:169], v[20:21] op_sel:[1,0,0] op_sel_hi:[1,1,1]
	v_pk_fma_f32 v[18:19], v[224:225], v[170:171], v[18:19] op_sel:[1,0,0] op_sel_hi:[1,1,1]
	v_pk_fma_f32 v[16:17], v[224:225], v[172:173], v[16:17] op_sel:[1,0,0] op_sel_hi:[1,1,1]
	v_pk_fma_f32 v[14:15], v[224:225], v[174:175], v[14:15] op_sel:[1,0,0] op_sel_hi:[1,1,1]
	v_pk_fma_f32 v[20:21], v[226:227], v[196:197], v[20:21] op_sel_hi:[0,1,1]
	v_pk_fma_f32 v[18:19], v[226:227], v[198:199], v[18:19] op_sel_hi:[0,1,1]
	v_pk_fma_f32 v[16:17], v[226:227], v[200:201], v[16:17] op_sel_hi:[0,1,1]
	v_pk_fma_f32 v[14:15], v[226:227], v[202:203], v[14:15] op_sel_hi:[0,1,1]
	v_pk_fma_f32 v[20:21], v[226:227], v[204:205], v[20:21] op_sel:[1,0,0] op_sel_hi:[1,1,1]
	v_pk_fma_f32 v[18:19], v[226:227], v[206:207], v[18:19] op_sel:[1,0,0] op_sel_hi:[1,1,1]
	v_pk_fma_f32 v[16:17], v[226:227], v[208:209], v[16:17] op_sel:[1,0,0] op_sel_hi:[1,1,1]
	v_pk_fma_f32 v[14:15], v[226:227], v[210:211], v[14:15] op_sel:[1,0,0] op_sel_hi:[1,1,1]
	s_add_i32 s19, s19, 1
	s_cmp_lt_u32 s19, 7
	s_cbranch_scc1 .LBB0_51
; __device__ void phase_prep(KParams& p, int bid, int nb, char* smem) {
;     ...
;       for (int mb = 0; mb < 256; mb += 16) {
;         float wv[16];
; #pragma unroll
;         for (int mm = 0; mm < 16; ++mm) wv[mm] = wp[(mb + mm) * 256];
; #pragma unroll
;         for (int mm = 0; mm < 16; ++mm) {
;           const int m = mb + mm;
;           const int p0 = (m * (cg * 4 + 0)) & 255, p1 = (m * (cg * 4 + 1)) & 255, p2 = (m * (cg * 4 + 2)) & 255, p3 = (m * (cg * 4 + 3)) & 255;
;           c0_ += t256[p0] * wv[mm]; s0_ += t256[(p0 - 64) & 255] * wv[mm];
;           c1_ += t256[p1] * wv[mm]; s1_ += t256[(p1 - 64) & 255] * wv[mm];
;           c2_ += t256[p2] * wv[mm]; s2_ += t256[(p2 - 64) & 255] * wv[mm];
;           c3_ += t256[p3] * wv[mm]; s3_ += t256[(p3 - 64) & 255] * wv[mm];
;         }
	v_add_co_u32_e32 v228, vcc, s15, v12
	s_nop 1
	v_addc_co_u32_e32 v229, vcc, -1, v13, vcc
	v_add_co_u32_e32 v230, vcc, s16, v12
	s_nop 1
	v_addc_co_u32_e32 v231, vcc, -1, v13, vcc
	v_add_co_u32_e32 v232, vcc, s17, v12
	s_nop 1
	v_addc_co_u32_e32 v233, vcc, -1, v13, vcc
	global_load_dword v226, v[12:13], off offset:-1024
	global_load_dword v227, v[12:13], off
	global_load_dword v212, v[228:229], off offset:-3072
	global_load_dword v213, v[228:229], off offset:-2048
	global_load_dword v214, v[228:229], off offset:-1024
	global_load_dword v220, v[232:233], off offset:-3072
	global_load_dword v221, v[232:233], off offset:-2048
	s_nop 0
	global_load_dword v222, v[232:233], off offset:-1024
	s_nop 0
	global_load_dword v215, v[230:231], off offset:-4096
	global_load_dword v216, v[230:231], off offset:-3072
	global_load_dword v217, v[230:231], off offset:-2048
	global_load_dword v218, v[230:231], off offset:-1024
	global_load_dword v219, v[230:231], off
	global_load_dword v223, v[12:13], off offset:-4096
	global_load_dword v224, v[12:13], off offset:-3072
	s_nop 0
	global_load_dword v225, v[12:13], off offset:-2048
	v_lshl_add_u64 v[12:13], v[12:13], 0, s[10:11]
	ds_read_b128 v[64:67], v60 offset:32768
	ds_read_b128 v[68:71], v60 offset:32784
	ds_read_b128 v[72:75], v60 offset:32800
	ds_read_b128 v[76:79], v60 offset:32816
	ds_read_b128 v[80:83], v60 offset:32832
	ds_read_b128 v[84:87], v60 offset:32848
	ds_read_b128 v[88:91], v60 offset:32864
	ds_read_b128 v[92:95], v60 offset:32880
	ds_read_b128 v[96:99], v60 offset:32896
	ds_read_b128 v[100:103], v60 offset:32912
	ds_read_b128 v[104:107], v60 offset:32928
	ds_read_b128 v[108:111], v60 offset:32944
	ds_read_b128 v[112:115], v60 offset:32960
	ds_read_b128 v[116:119], v60 offset:32976
	ds_read_b128 v[120:123], v60 offset:32992
	ds_read_b128 v[124:127], v60 offset:33008
	ds_read_b128 v[128:131], v60 offset:33024
	ds_read_b128 v[132:135], v60 offset:33040
	ds_read_b128 v[136:139], v60 offset:33056
	ds_read_b128 v[140:143], v60 offset:33072
	ds_read_b128 v[144:147], v60 offset:33088
	ds_read_b128 v[148:151], v60 offset:33104
	ds_read_b128 v[152:155], v60 offset:33120
	ds_read_b128 v[156:159], v60 offset:33136
	ds_read_b128 v[160:163], v60 offset:33152
	ds_read_b128 v[164:167], v60 offset:33168
	ds_read_b128 v[168:171], v60 offset:33184
	ds_read_b128 v[172:175], v60 offset:33200
	ds_read_b128 v[196:199], v60 offset:33216
	ds_read_b128 v[200:203], v60 offset:33232
	ds_read_b128 v[204:207], v60 offset:33248
	ds_read_b128 v[208:211], v60 offset:33264
	v_add_u32_e32 v60, 0x200, v60
	s_waitcnt vmcnt(16) lgkmcnt(0)
	v_pk_fma_f32 v[20:21], v[50:51], v[64:65], v[20:21] op_sel_hi:[0,1,1]
	v_pk_fma_f32 v[18:19], v[50:51], v[66:67], v[18:19] op_sel_hi:[0,1,1]
	v_pk_fma_f32 v[16:17], v[50:51], v[68:69], v[16:17] op_sel_hi:[0,1,1]
	v_pk_fma_f32 v[14:15], v[50:51], v[70:71], v[14:15] op_sel_hi:[0,1,1]
	v_pk_fma_f32 v[20:21], v[48:49], v[72:73], v[20:21] op_sel_hi:[0,1,1]
	v_pk_fma_f32 v[18:19], v[48:49], v[74:75], v[18:19] op_sel_hi:[0,1,1]
	v_pk_fma_f32 v[16:17], v[48:49], v[76:77], v[16:17] op_sel_hi:[0,1,1]
	v_pk_fma_f32 v[14:15], v[48:49], v[78:79], v[14:15] op_sel_hi:[0,1,1]
	v_pk_fma_f32 v[20:21], v[44:45], v[80:81], v[20:21] op_sel_hi:[0,1,1]
	v_pk_fma_f32 v[18:19], v[44:45], v[82:83], v[18:19] op_sel_hi:[0,1,1]
	v_pk_fma_f32 v[16:17], v[44:45], v[84:85], v[16:17] op_sel_hi:[0,1,1]
	v_pk_fma_f32 v[14:15], v[44:45], v[86:87], v[14:15] op_sel_hi:[0,1,1]
	v_pk_fma_f32 v[20:21], v[46:47], v[88:89], v[20:21] op_sel_hi:[0,1,1]
	v_pk_fma_f32 v[18:19], v[46:47], v[90:91], v[18:19] op_sel_hi:[0,1,1]
	v_pk_fma_f32 v[16:17], v[46:47], v[92:93], v[16:17] op_sel_hi:[0,1,1]
	v_pk_fma_f32 v[14:15], v[46:47], v[94:95], v[14:15] op_sel_hi:[0,1,1]
	v_pk_fma_f32 v[20:21], v[42:43], v[96:97], v[20:21] op_sel_hi:[0,1,1]
	v_pk_fma_f32 v[18:19], v[42:43], v[98:99], v[18:19] op_sel_hi:[0,1,1]
	v_pk_fma_f32 v[16:17], v[42:43], v[100:101], v[16:17] op_sel_hi:[0,1,1]
	v_pk_fma_f32 v[14:15], v[42:43], v[102:103], v[14:15] op_sel_hi:[0,1,1]
	v_pk_fma_f32 v[20:21], v[40:41], v[104:105], v[20:21] op_sel_hi:[0,1,1]
	v_pk_fma_f32 v[18:19], v[40:41], v[106:107], v[18:19] op_sel_hi:[0,1,1]
	v_pk_fma_f32 v[16:17], v[40:41], v[108:109], v[16:17] op_sel_hi:[0,1,1]
	v_pk_fma_f32 v[14:15], v[40:41], v[110:111], v[14:15] op_sel_hi:[0,1,1]
	v_pk_fma_f32 v[20:21], v[38:39], v[112:113], v[20:21] op_sel_hi:[0,1,1]
	v_pk_fma_f32 v[18:19], v[38:39], v[114:115], v[18:19] op_sel_hi:[0,1,1]
	v_pk_fma_f32 v[16:17], v[38:39], v[116:117], v[16:17] op_sel_hi:[0,1,1]
	v_pk_fma_f32 v[14:15], v[38:39], v[118:119], v[14:15] op_sel_hi:[0,1,1]
	v_pk_fma_f32 v[20:21], v[36:37], v[120:121], v[20:21] op_sel_hi:[0,1,1]
	v_pk_fma_f32 v[18:19], v[36:37], v[122:123], v[18:19] op_sel_hi:[0,1,1]
	v_pk_fma_f32 v[16:17], v[36:37], v[124:125], v[16:17] op_sel_hi:[0,1,1]
	v_pk_fma_f32 v[14:15], v[36:37], v[126:127], v[14:15] op_sel_hi:[0,1,1]
	v_pk_fma_f32 v[20:21], v[34:35], v[128:129], v[20:21] op_sel_hi:[0,1,1]
	v_pk_fma_f32 v[18:19], v[34:35], v[130:131], v[18:19] op_sel_hi:[0,1,1]
	v_pk_fma_f32 v[16:17], v[34:35], v[132:133], v[16:17] op_sel_hi:[0,1,1]
	v_pk_fma_f32 v[14:15], v[34:35], v[134:135], v[14:15] op_sel_hi:[0,1,1]
	v_pk_fma_f32 v[20:21], v[32:33], v[136:137], v[20:21] op_sel_hi:[0,1,1]
	v_pk_fma_f32 v[18:19], v[32:33], v[138:139], v[18:19] op_sel_hi:[0,1,1]
	v_pk_fma_f32 v[16:17], v[32:33], v[140:141], v[16:17] op_sel_hi:[0,1,1]
	v_pk_fma_f32 v[14:15], v[32:33], v[142:143], v[14:15] op_sel_hi:[0,1,1]
	v_pk_fma_f32 v[20:21], v[28:29], v[144:145], v[20:21] op_sel_hi:[0,1,1]
	v_pk_fma_f32 v[18:19], v[28:29], v[146:147], v[18:19] op_sel_hi:[0,1,1]
; __device__ void phase_prep(KParams& p, int bid, int nb, char* smem) {
;     ...
;       for (int mb = 0; mb < 256; mb += 16) {
;         float wv[16];
; #pragma unroll
;         for (int mm = 0; mm < 16; ++mm) wv[mm] = wp[(mb + mm) * 256];
; #pragma unroll
;         for (int mm = 0; mm < 16; ++mm) {
;           const int m = mb + mm;
;           const int p0 = (m * (cg * 4 + 0)) & 255, p1 = (m * (cg * 4 + 1)) & 255, p2 = (m * (cg * 4 + 2)) & 255, p3 = (m * (cg * 4 + 3)) & 255;
;           c0_ += t256[p0] * wv[mm]; s0_ += t256[(p0 - 64) & 255] * wv[mm];
;           c1_ += t256[p1] * wv[mm]; s1_ += t256[(p1 - 64) & 255] * wv[mm];
;           c2_ += t256[p2] * wv[mm]; s2_ += t256[(p2 - 64) & 255] * wv[mm];
;           c3_ += t256[p3] * wv[mm]; s3_ += t256[(p3 - 64) & 255] * wv[mm];
;         }
	v_pk_fma_f32 v[16:17], v[28:29], v[148:149], v[16:17] op_sel_hi:[0,1,1]
	v_pk_fma_f32 v[14:15], v[28:29], v[150:151], v[14:15] op_sel_hi:[0,1,1]
	v_pk_fma_f32 v[20:21], v[30:31], v[152:153], v[20:21] op_sel_hi:[0,1,1]
	v_pk_fma_f32 v[18:19], v[30:31], v[154:155], v[18:19] op_sel_hi:[0,1,1]
	v_pk_fma_f32 v[16:17], v[30:31], v[156:157], v[16:17] op_sel_hi:[0,1,1]
	v_pk_fma_f32 v[14:15], v[30:31], v[158:159], v[14:15] op_sel_hi:[0,1,1]
	v_pk_fma_f32 v[20:21], v[26:27], v[160:161], v[20:21] op_sel_hi:[0,1,1]
	v_pk_fma_f32 v[18:19], v[26:27], v[162:163], v[18:19] op_sel_hi:[0,1,1]
	v_pk_fma_f32 v[16:17], v[26:27], v[164:165], v[16:17] op_sel_hi:[0,1,1]
	v_pk_fma_f32 v[14:15], v[26:27], v[166:167], v[14:15] op_sel_hi:[0,1,1]
	v_pk_fma_f32 v[20:21], v[24:25], v[168:169], v[20:21] op_sel_hi:[0,1,1]
	v_pk_fma_f32 v[18:19], v[24:25], v[170:171], v[18:19] op_sel_hi:[0,1,1]
	v_pk_fma_f32 v[16:17], v[24:25], v[172:173], v[16:17] op_sel_hi:[0,1,1]
	v_pk_fma_f32 v[14:15], v[24:25], v[174:175], v[14:15] op_sel_hi:[0,1,1]
	v_pk_fma_f32 v[20:21], v[22:23], v[196:197], v[20:21] op_sel_hi:[0,1,1]
	v_pk_fma_f32 v[18:19], v[22:23], v[198:199], v[18:19] op_sel_hi:[0,1,1]
	v_pk_fma_f32 v[16:17], v[22:23], v[200:201], v[16:17] op_sel_hi:[0,1,1]
	v_pk_fma_f32 v[14:15], v[22:23], v[202:203], v[14:15] op_sel_hi:[0,1,1]
	v_pk_fma_f32 v[20:21], v[2:3], v[204:205], v[20:21] op_sel_hi:[0,1,1]
	v_pk_fma_f32 v[18:19], v[2:3], v[206:207], v[18:19] op_sel_hi:[0,1,1]
	v_pk_fma_f32 v[16:17], v[2:3], v[208:209], v[16:17] op_sel_hi:[0,1,1]
	v_pk_fma_f32 v[14:15], v[2:3], v[210:211], v[14:15] op_sel_hi:[0,1,1]
	ds_read_b128 v[64:67], v60 offset:32768
	ds_read_b128 v[68:71], v60 offset:32784
	ds_read_b128 v[72:75], v60 offset:32800
	ds_read_b128 v[76:79], v60 offset:32816
	ds_read_b128 v[80:83], v60 offset:32832
	ds_read_b128 v[84:87], v60 offset:32848
	ds_read_b128 v[88:91], v60 offset:32864
	ds_read_b128 v[92:95], v60 offset:32880
	ds_read_b128 v[96:99], v60 offset:32896
	ds_read_b128 v[100:103], v60 offset:32912
	ds_read_b128 v[104:107], v60 offset:32928
	ds_read_b128 v[108:111], v60 offset:32944
	ds_read_b128 v[112:115], v60 offset:32960
	ds_read_b128 v[116:119], v60 offset:32976
	ds_read_b128 v[120:123], v60 offset:32992
	ds_read_b128 v[124:127], v60 offset:33008
	ds_read_b128 v[128:131], v60 offset:33024
	ds_read_b128 v[132:135], v60 offset:33040
	ds_read_b128 v[136:139], v60 offset:33056
	ds_read_b128 v[140:143], v60 offset:33072
	ds_read_b128 v[144:147], v60 offset:33088
	ds_read_b128 v[148:151], v60 offset:33104
	ds_read_b128 v[152:155], v60 offset:33120
	ds_read_b128 v[156:159], v60 offset:33136
	ds_read_b128 v[160:163], v60 offset:33152
	ds_read_b128 v[164:167], v60 offset:33168
	ds_read_b128 v[168:171], v60 offset:33184
	ds_read_b128 v[172:175], v60 offset:33200
	ds_read_b128 v[196:199], v60 offset:33216
	ds_read_b128 v[200:203], v60 offset:33232
	ds_read_b128 v[204:207], v60 offset:33248
	ds_read_b128 v[208:211], v60 offset:33264
	v_add_u32_e32 v60, 0x200, v60
	s_waitcnt vmcnt(0) lgkmcnt(0)
; __device__ void phase_prep(KParams& p, int bid, int nb, char* smem) {
;     ...
;       for (int mb = 0; mb < 256; mb += 16) {
;         float wv[16];
; #pragma unroll
;         for (int mm = 0; mm < 16; ++mm) wv[mm] = wp[(mb + mm) * 256];
; #pragma unroll
;         for (int mm = 0; mm < 16; ++mm) {
;           const int m = mb + mm;
;           const int p0 = (m * (cg * 4 + 0)) & 255, p1 = (m * (cg * 4 + 1)) & 255, p2 = (m * (cg * 4 + 2)) & 255, p3 = (m * (cg * 4 + 3)) & 255;
;           c0_ += t256[p0] * wv[mm]; s0_ += t256[(p0 - 64) & 255] * wv[mm];
;           c1_ += t256[p1] * wv[mm]; s1_ += t256[(p1 - 64) & 255] * wv[mm];
;           c2_ += t256[p2] * wv[mm]; s2_ += t256[(p2 - 64) & 255] * wv[mm];
;           c3_ += t256[p3] * wv[mm]; s3_ += t256[(p3 - 64) & 255] * wv[mm];
;         }
;       }
;       {
;         bf16_t* wc = p.WcsT + ((size_t)g * 512 + d) * 256 + cg * 4;
;         bf16_t* ws_ = p.WcsT + ((size_t)g * 512 + 256 + d) * 256 + cg * 4;
;         uint2 oc, os;
;         oc.x = pack2(c0_ * scale, c1_ * scale); oc.y = pack2(c2_ * scale, c3_ * scale);
;         os.x = pack2(s0_ * scale, s1_ * scale); os.y = pack2(s2_ * scale, s3_ * scale);
;         *reinterpret_cast<uint2*>(wc) = oc;
;         *reinterpret_cast<uint2*>(ws_) = os;
;       }
	v_pk_fma_f32 v[20:21], v[212:213], v[64:65], v[20:21] op_sel_hi:[0,1,1]
	v_pk_fma_f32 v[18:19], v[212:213], v[66:67], v[18:19] op_sel_hi:[0,1,1]
	v_pk_fma_f32 v[16:17], v[212:213], v[68:69], v[16:17] op_sel_hi:[0,1,1]
	v_pk_fma_f32 v[14:15], v[212:213], v[70:71], v[14:15] op_sel_hi:[0,1,1]
	v_pk_fma_f32 v[20:21], v[212:213], v[72:73], v[20:21] op_sel:[1,0,0] op_sel_hi:[1,1,1]
	v_pk_fma_f32 v[18:19], v[212:213], v[74:75], v[18:19] op_sel:[1,0,0] op_sel_hi:[1,1,1]
	v_pk_fma_f32 v[16:17], v[212:213], v[76:77], v[16:17] op_sel:[1,0,0] op_sel_hi:[1,1,1]
	v_pk_fma_f32 v[14:15], v[212:213], v[78:79], v[14:15] op_sel:[1,0,0] op_sel_hi:[1,1,1]
	v_pk_fma_f32 v[20:21], v[214:215], v[80:81], v[20:21] op_sel_hi:[0,1,1]
	v_pk_fma_f32 v[18:19], v[214:215], v[82:83], v[18:19] op_sel_hi:[0,1,1]
	v_pk_fma_f32 v[16:17], v[214:215], v[84:85], v[16:17] op_sel_hi:[0,1,1]
	v_pk_fma_f32 v[14:15], v[214:215], v[86:87], v[14:15] op_sel_hi:[0,1,1]
	v_pk_fma_f32 v[20:21], v[214:215], v[88:89], v[20:21] op_sel:[1,0,0] op_sel_hi:[1,1,1]
	v_pk_fma_f32 v[18:19], v[214:215], v[90:91], v[18:19] op_sel:[1,0,0] op_sel_hi:[1,1,1]
	v_pk_fma_f32 v[16:17], v[214:215], v[92:93], v[16:17] op_sel:[1,0,0] op_sel_hi:[1,1,1]
	v_pk_fma_f32 v[14:15], v[214:215], v[94:95], v[14:15] op_sel:[1,0,0] op_sel_hi:[1,1,1]
	v_pk_fma_f32 v[20:21], v[216:217], v[96:97], v[20:21] op_sel_hi:[0,1,1]
	v_pk_fma_f32 v[18:19], v[216:217], v[98:99], v[18:19] op_sel_hi:[0,1,1]
	v_pk_fma_f32 v[16:17], v[216:217], v[100:101], v[16:17] op_sel_hi:[0,1,1]
	v_pk_fma_f32 v[14:15], v[216:217], v[102:103], v[14:15] op_sel_hi:[0,1,1]
	v_pk_fma_f32 v[20:21], v[216:217], v[104:105], v[20:21] op_sel:[1,0,0] op_sel_hi:[1,1,1]
	v_pk_fma_f32 v[18:19], v[216:217], v[106:107], v[18:19] op_sel:[1,0,0] op_sel_hi:[1,1,1]
	v_pk_fma_f32 v[16:17], v[216:217], v[108:109], v[16:17] op_sel:[1,0,0] op_sel_hi:[1,1,1]
	v_pk_fma_f32 v[14:15], v[216:217], v[110:111], v[14:15] op_sel:[1,0,0] op_sel_hi:[1,1,1]
	v_pk_fma_f32 v[20:21], v[218:219], v[112:113], v[20:21] op_sel_hi:[0,1,1]
	v_pk_fma_f32 v[18:19], v[218:219], v[114:115], v[18:19] op_sel_hi:[0,1,1]
	v_pk_fma_f32 v[16:17], v[218:219], v[116:117], v[16:17] op_sel_hi:[0,1,1]
	v_pk_fma_f32 v[14:15], v[218:219], v[118:119], v[14:15] op_sel_hi:[0,1,1]
	v_pk_fma_f32 v[20:21], v[218:219], v[120:121], v[20:21] op_sel:[1,0,0] op_sel_hi:[1,1,1]
	v_pk_fma_f32 v[18:19], v[218:219], v[122:123], v[18:19] op_sel:[1,0,0] op_sel_hi:[1,1,1]
	v_pk_fma_f32 v[16:17], v[218:219], v[124:125], v[16:17] op_sel:[1,0,0] op_sel_hi:[1,1,1]
	v_pk_fma_f32 v[14:15], v[218:219], v[126:127], v[14:15] op_sel:[1,0,0] op_sel_hi:[1,1,1]
	v_pk_fma_f32 v[20:21], v[220:221], v[128:129], v[20:21] op_sel_hi:[0,1,1]
	v_pk_fma_f32 v[18:19], v[220:221], v[130:131], v[18:19] op_sel_hi:[0,1,1]
	v_pk_fma_f32 v[16:17], v[220:221], v[132:133], v[16:17] op_sel_hi:[0,1,1]
	v_pk_fma_f32 v[14:15], v[220:221], v[134:135], v[14:15] op_sel_hi:[0,1,1]
	v_pk_fma_f32 v[20:21], v[220:221], v[136:137], v[20:21] op_sel:[1,0,0] op_sel_hi:[1,1,1]
	v_pk_fma_f32 v[18:19], v[220:221], v[138:139], v[18:19] op_sel:[1,0,0] op_sel_hi:[1,1,1]
	v_pk_fma_f32 v[16:17], v[220:221], v[140:141], v[16:17] op_sel:[1,0,0] op_sel_hi:[1,1,1]
	v_pk_fma_f32 v[14:15], v[220:221], v[142:143], v[14:15] op_sel:[1,0,0] op_sel_hi:[1,1,1]
	v_pk_fma_f32 v[20:21], v[222:223], v[144:145], v[20:21] op_sel_hi:[0,1,1]
	v_pk_fma_f32 v[18:19], v[222:223], v[146:147], v[18:19] op_sel_hi:[0,1,1]
	v_pk_fma_f32 v[16:17], v[222:223], v[148:149], v[16:17] op_sel_hi:[0,1,1]
	v_pk_fma_f32 v[14:15], v[222:223], v[150:151], v[14:15] op_sel_hi:[0,1,1]
	v_pk_fma_f32 v[20:21], v[222:223], v[152:153], v[20:21] op_sel:[1,0,0] op_sel_hi:[1,1,1]
	v_pk_fma_f32 v[18:19], v[222:223], v[154:155], v[18:19] op_sel:[1,0,0] op_sel_hi:[1,1,1]
	v_pk_fma_f32 v[16:17], v[222:223], v[156:157], v[16:17] op_sel:[1,0,0] op_sel_hi:[1,1,1]
	v_pk_fma_f32 v[14:15], v[222:223], v[158:159], v[14:15] op_sel:[1,0,0] op_sel_hi:[1,1,1]
	v_pk_fma_f32 v[20:21], v[224:225], v[160:161], v[20:21] op_sel_hi:[0,1,1]
	v_pk_fma_f32 v[18:19], v[224:225], v[162:163], v[18:19] op_sel_hi:[0,1,1]
	v_pk_fma_f32 v[16:17], v[224:225], v[164:165], v[16:17] op_sel_hi:[0,1,1]
	v_pk_fma_f32 v[14:15], v[224:225], v[166:167], v[14:15] op_sel_hi:[0,1,1]
	v_pk_fma_f32 v[20:21], v[224:225], v[168:169], v[20:21] op_sel:[1,0,0] op_sel_hi:[1,1,1]
	v_pk_fma_f32 v[18:19], v[224:225], v[170:171], v[18:19] op_sel:[1,0,0] op_sel_hi:[1,1,1]
	v_pk_fma_f32 v[16:17], v[224:225], v[172:173], v[16:17] op_sel:[1,0,0] op_sel_hi:[1,1,1]
	v_pk_fma_f32 v[14:15], v[224:225], v[174:175], v[14:15] op_sel:[1,0,0] op_sel_hi:[1,1,1]
	v_pk_fma_f32 v[20:21], v[226:227], v[196:197], v[20:21] op_sel_hi:[0,1,1]
	v_pk_fma_f32 v[18:19], v[226:227], v[198:199], v[18:19] op_sel_hi:[0,1,1]
	v_pk_fma_f32 v[16:17], v[226:227], v[200:201], v[16:17] op_sel_hi:[0,1,1]
	v_pk_fma_f32 v[14:15], v[226:227], v[202:203], v[14:15] op_sel_hi:[0,1,1]
	v_pk_fma_f32 v[20:21], v[226:227], v[204:205], v[20:21] op_sel:[1,0,0] op_sel_hi:[1,1,1]
	v_pk_fma_f32 v[18:19], v[226:227], v[206:207], v[18:19] op_sel:[1,0,0] op_sel_hi:[1,1,1]
	v_pk_fma_f32 v[16:17], v[226:227], v[208:209], v[16:17] op_sel:[1,0,0] op_sel_hi:[1,1,1]
	v_pk_fma_f32 v[14:15], v[226:227], v[210:211], v[14:15] op_sel:[1,0,0] op_sel_hi:[1,1,1]
	v_lshrrev_b32_e32 v2, 5, v1
	v_lshl_add_u64 v[10:11], v[4:5], 0, v[10:11]
	v_and_b32_e32 v2, 0x1f8, v2
	v_pk_mul_f32 v[12:13], v[20:21], s[14:15] op_sel_hi:[1,0]
	v_pk_mul_f32 v[16:17], v[16:17], s[14:15] op_sel_hi:[1,0]
	v_lshl_add_u64 v[10:11], v[10:11], 0, v[2:3]
	v_cvt_pk_bf16_f32 v12, v12, v13
	v_cvt_pk_bf16_f32 v13, v16, v17
	global_store_dwordx2 v[10:11], v[12:13], off
	v_add_co_u32_e32 v10, vcc, 0x20000, v10
	v_add_u32_e32 v1, s3, v1
	s_nop 0
	v_addc_co_u32_e32 v11, vcc, 0, v11, vcc
	v_pk_mul_f32 v[16:17], v[18:19], s[14:15] op_sel_hi:[1,0]
	v_pk_mul_f32 v[14:15], v[14:15], s[14:15] op_sel_hi:[1,0]
	v_cmp_lt_i32_e32 vcc, s18, v1
	v_cvt_pk_bf16_f32 v16, v16, v17
	v_cvt_pk_bf16_f32 v17, v14, v15
	s_or_b64 s[8:9], vcc, s[8:9]
	global_store_dwordx2 v[10:11], v[16:17], off
	s_andn2_b64 exec, exec, s[8:9]
	s_cbranch_execnz .LBB0_50
